# baseline (speedup 1.0000x reference)
_Z9fc_kernelPKDv8_DF16_S1_Pf:
	s_cmp_gt_u32 s2, 195
	s_cbranch_scc1 .Lfc_exit
	s_load_dwordx4 s[4:7], s[0:1], 0x0
	s_load_dwordx2 s[16:17], s[0:1], 0x10
	v_and_b32_e32 v1, 63, v0
	v_lshrrev_b32_e32 v113, 6, v0
	v_and_b32_e32 v89, 31, v0
	v_bfe_u32 v90, v0, 5, 1
	v_lshlrev_b32_e32 v116, 4, v0
	v_lshlrev_b32_e32 v112, 4, v1
	v_lshlrev_b32_e32 v4, 12, v90
	v_lshl_or_b32 v4, v113, 8, v4
	v_lshl_or_b32 v4, v89, 2, v4
	v_add_u32_e32 v102, 0x1c000, v4
	v_lshlrev_b32_e32 v5, 13, v113
	s_mov_b32 s3, 0x1c000
	v_add3_u32 v103, v5, v112, s3
	v_mul_u32_u24_e32 v6, 0x186a00, v113
	v_add_u32_e32 v104, v6, v112
	v_add_u32_e32 v105, 0x30d40, v104
	v_add_u32_e32 v106, 0x61a80, v104
	v_add_u32_e32 v107, 0x927c0, v104
	v_add_u32_e32 v108, 0xc3500, v104
	v_add_u32_e32 v109, 0xf4240, v104
	v_add_u32_e32 v110, 0x124f80, v104
	v_add_u32_e32 v111, 0x155cc0, v104
	v_mul_u32_u24_e32 v7, 0x3800, v113
	v_add_u32_e32 v114, v7, v112
	v_cmp_gt_u32_e64 s[34:35], 20, v1
	v_readfirstlane_b32 s38, v113
	s_lshl_b32 s46, s38, 10
	s_mul_i32 s3, s2, 0xe000
	v_add_u32_e32 v117, s3, v114
	v_add_u32_e32 v118, 0x1000, v117
	v_add_u32_e32 v119, 0x2000, v117
	v_add_u32_e32 v115, 0x3000, v117
	s_waitcnt lgkmcnt(0)
	global_load_dwordx4 v[32:35], v117, s[4:5]
	global_load_dwordx4 v[36:39], v117, s[4:5] offset:1024
	global_load_dwordx4 v[40:43], v117, s[4:5] offset:2048
	global_load_dwordx4 v[44:47], v117, s[4:5] offset:3072
	global_load_dwordx4 v[48:51], v118, s[4:5]
	global_load_dwordx4 v[52:55], v118, s[4:5] offset:1024
	global_load_dwordx4 v[56:59], v118, s[4:5] offset:2048
	global_load_dwordx4 v[60:63], v118, s[4:5] offset:3072
	global_load_dwordx4 v[64:67], v119, s[4:5]
	global_load_dwordx4 v[68:71], v119, s[4:5] offset:1024
	global_load_dwordx4 v[72:75], v119, s[4:5] offset:2048
	global_load_dwordx4 v[76:79], v119, s[4:5] offset:3072
	global_load_dwordx4 v[80:83], v115, s[4:5]
	global_load_dwordx4 v[84:87], v115, s[4:5] offset:1024
	s_mov_b64 s[30:31], s[6:7]
	s_mov_b32 s3, s46
	s_mov_b32 m0, s3
	s_nop 0
	global_load_lds_dwordx4 v116, s[30:31]
	s_add_u32 s30, s30, 0x1000
	s_addc_u32 s31, s31, 0
	s_add_u32 m0, s3, 0x1000
	s_nop 0
	global_load_lds_dwordx4 v116, s[30:31]
	s_add_u32 s30, s30, 0x1000
	s_addc_u32 s31, s31, 0
	s_add_u32 m0, s3, 0x2000
	s_nop 0
	global_load_lds_dwordx4 v116, s[30:31]
	s_add_u32 s30, s30, 0x1000
	s_addc_u32 s31, s31, 0
	s_add_u32 m0, s3, 0x3000
	s_nop 0
	global_load_lds_dwordx4 v116, s[30:31]
	s_add_u32 s30, s30, 0x1000
	s_addc_u32 s31, s31, 0
	s_add_u32 m0, s3, 0x4000
	s_nop 0
	global_load_lds_dwordx4 v116, s[30:31]
	s_add_u32 s30, s30, 0x1000
	s_addc_u32 s31, s31, 0
	s_add_u32 m0, s3, 0x5000
	s_nop 0
	global_load_lds_dwordx4 v116, s[30:31]
	s_add_u32 s30, s30, 0x1000
	s_addc_u32 s31, s31, 0
	s_add_u32 m0, s3, 0x6000
	s_nop 0
	global_load_lds_dwordx4 v116, s[30:31]
	s_add_u32 s30, s30, 0x1000
	s_addc_u32 s31, s31, 0
	s_add_u32 m0, s3, 0x7000
	s_nop 0
	global_load_lds_dwordx4 v116, s[30:31]
	s_add_u32 s30, s30, 0x1000
	s_addc_u32 s31, s31, 0
	s_add_u32 m0, s3, 0x8000
	s_nop 0
	global_load_lds_dwordx4 v116, s[30:31]
	s_add_u32 s30, s30, 0x1000
	s_addc_u32 s31, s31, 0
	s_add_u32 m0, s3, 0x9000
	s_nop 0
	global_load_lds_dwordx4 v116, s[30:31]
	s_add_u32 s30, s30, 0x1000
	s_addc_u32 s31, s31, 0
	s_add_u32 m0, s3, 0xa000
	s_nop 0
	global_load_lds_dwordx4 v116, s[30:31]
	s_add_u32 s30, s30, 0x1000
	s_addc_u32 s31, s31, 0
	s_add_u32 m0, s3, 0xb000
	s_nop 0
	global_load_lds_dwordx4 v116, s[30:31]
	s_add_u32 s30, s30, 0x1000
	s_addc_u32 s31, s31, 0
	s_add_u32 m0, s3, 0xc000
	s_nop 0
	global_load_lds_dwordx4 v116, s[30:31]
	s_add_u32 s30, s30, 0x1000
	s_addc_u32 s31, s31, 0
	s_add_u32 m0, s3, 0xd000
	s_nop 0
	global_load_lds_dwordx4 v116, s[30:31]
	s_lshl_b32 s3, s2, 10
	s_add_u32 s8, s16, s3
	s_addc_u32 s9, s17, 0
	s_mov_b64 s[24:25], -1
	s_cmp_eq_u32 s2, 195
	s_cselect_b64 s[24:25], s[34:35], s[24:25]
	s_mov_b32 s20, 0
	s_waitcnt vmcnt(0)
	s_barrier
.Lfc_seg:
	s_cmp_eq_u32 s20, 15
	s_cbranch_scc1 .Lfc_nopf
	s_add_i32 s3, s20, 1
	s_mul_i32 s3, s3, 0xe000
	s_add_u32 s30, s6, s3
	s_addc_u32 s31, s7, 0
	s_add_i32 s3, s20, 1
	s_and_b32 s3, s3, 1
	s_mul_i32 s3, s3, 0xe000
	s_add_i32 s3, s3, s46
	s_mov_b32 m0, s3
	s_nop 0
	global_load_lds_dwordx4 v116, s[30:31]
	s_add_u32 s30, s30, 0x1000
	s_addc_u32 s31, s31, 0
	s_add_u32 m0, s3, 0x1000
	s_nop 0
	global_load_lds_dwordx4 v116, s[30:31]
	s_add_u32 s30, s30, 0x1000
	s_addc_u32 s31, s31, 0
	s_add_u32 m0, s3, 0x2000
	s_nop 0
	global_load_lds_dwordx4 v116, s[30:31]
	s_add_u32 s30, s30, 0x1000
	s_addc_u32 s31, s31, 0
	s_add_u32 m0, s3, 0x3000
	s_nop 0
	global_load_lds_dwordx4 v116, s[30:31]
	s_add_u32 s30, s30, 0x1000
	s_addc_u32 s31, s31, 0
	s_add_u32 m0, s3, 0x4000
	s_nop 0
	global_load_lds_dwordx4 v116, s[30:31]
	s_add_u32 s30, s30, 0x1000
	s_addc_u32 s31, s31, 0
	s_add_u32 m0, s3, 0x5000
	s_nop 0
	global_load_lds_dwordx4 v116, s[30:31]
	s_add_u32 s30, s30, 0x1000
	s_addc_u32 s31, s31, 0
	s_add_u32 m0, s3, 0x6000
	s_nop 0
	global_load_lds_dwordx4 v116, s[30:31]
	s_add_u32 s30, s30, 0x1000
	s_addc_u32 s31, s31, 0
	s_add_u32 m0, s3, 0x7000
	s_nop 0
	global_load_lds_dwordx4 v116, s[30:31]
	s_add_u32 s30, s30, 0x1000
	s_addc_u32 s31, s31, 0
	s_add_u32 m0, s3, 0x8000
	s_nop 0
	global_load_lds_dwordx4 v116, s[30:31]
	s_add_u32 s30, s30, 0x1000
	s_addc_u32 s31, s31, 0
	s_add_u32 m0, s3, 0x9000
	s_nop 0
	global_load_lds_dwordx4 v116, s[30:31]
	s_add_u32 s30, s30, 0x1000
	s_addc_u32 s31, s31, 0
	s_add_u32 m0, s3, 0xa000
	s_nop 0
	global_load_lds_dwordx4 v116, s[30:31]
	s_add_u32 s30, s30, 0x1000
	s_addc_u32 s31, s31, 0
	s_add_u32 m0, s3, 0xb000
	s_nop 0
	global_load_lds_dwordx4 v116, s[30:31]
	s_add_u32 s30, s30, 0x1000
	s_addc_u32 s31, s31, 0
	s_add_u32 m0, s3, 0xc000
	s_nop 0
	global_load_lds_dwordx4 v116, s[30:31]
	s_add_u32 s30, s30, 0x1000
	s_addc_u32 s31, s31, 0
	s_add_u32 m0, s3, 0xd000
	s_nop 0
	global_load_lds_dwordx4 v116, s[30:31]

.Lfc_step:
	v_mfma_f32_32x32x16_f16 v[0:15], v[120:123], v[32:35], 0
	v_mfma_f32_32x32x16_f16 v[16:31], v[120:123], v[60:63], 0
	v_mfma_f32_32x32x16_f16 v[0:15], v[124:127], v[36:39], v[0:15]
	v_mfma_f32_32x32x16_f16 v[16:31], v[124:127], v[64:67], v[16:31]
	v_mfma_f32_32x32x16_f16 v[0:15], v[128:131], v[40:43], v[0:15]
	v_mfma_f32_32x32x16_f16 v[16:31], v[128:131], v[68:71], v[16:31]
	v_mfma_f32_32x32x16_f16 v[0:15], v[132:135], v[44:47], v[0:15]
	v_mfma_f32_32x32x16_f16 v[16:31], v[132:135], v[72:75], v[16:31]
	v_mfma_f32_32x32x16_f16 v[0:15], v[136:139], v[48:51], v[0:15]
	v_mfma_f32_32x32x16_f16 v[16:31], v[136:139], v[76:79], v[16:31]
	v_mfma_f32_32x32x16_f16 v[0:15], v[140:143], v[52:55], v[0:15]
	v_mfma_f32_32x32x16_f16 v[16:31], v[140:143], v[80:83], v[16:31]
	v_mfma_f32_32x32x16_f16 v[0:15], v[144:147], v[56:59], v[0:15]
	v_mfma_f32_32x32x16_f16 v[16:31], v[144:147], v[84:87], v[16:31]
	s_nop 11
	s_barrier
	ds_write_b32 v102, v0 offset:0
	ds_write_b32 v102, v1 offset:1024
	ds_write_b32 v102, v2 offset:2048
	ds_write_b32 v102, v3 offset:3072
	ds_write_b32 v102, v4 offset:8192
	ds_write_b32 v102, v5 offset:9216
	ds_write_b32 v102, v6 offset:10240
	ds_write_b32 v102, v7 offset:11264
	ds_write_b32 v102, v8 offset:16384
	ds_write_b32 v102, v9 offset:17408
	ds_write_b32 v102, v10 offset:18432
	ds_write_b32 v102, v11 offset:19456
	ds_write_b32 v102, v12 offset:24576
	ds_write_b32 v102, v13 offset:25600
	ds_write_b32 v102, v14 offset:26624
	ds_write_b32 v102, v15 offset:27648
	ds_write_b32 v102, v16 offset:128
	ds_write_b32 v102, v17 offset:1152
	ds_write_b32 v102, v18 offset:2176
	ds_write_b32 v102, v19 offset:3200
	ds_write_b32 v102, v20 offset:8320
	ds_write_b32 v102, v21 offset:9344
	ds_write_b32 v102, v22 offset:10368
	ds_write_b32 v102, v23 offset:11392
	ds_write_b32 v102, v24 offset:16512
	ds_write_b32 v102, v25 offset:17536
	ds_write_b32 v102, v26 offset:18560
	ds_write_b32 v102, v27 offset:19584
	ds_write_b32 v102, v28 offset:24704
	ds_write_b32 v102, v29 offset:25728
	ds_write_b32 v102, v30 offset:26752
	ds_write_b32 v102, v31 offset:27776
	s_waitcnt lgkmcnt(0)
	s_barrier
	ds_read_b128 v[120:123], v88
	ds_read_b128 v[124:127], v88 offset:1024
	ds_read_b128 v[128:131], v88 offset:2048
	ds_read_b128 v[132:135], v88 offset:3072
	ds_read_b128 v[136:139], v88 offset:4096
	ds_read_b128 v[140:143], v88 offset:5120
	ds_read_b128 v[144:147], v88 offset:6144
	v_add_u32_e32 v88, 0x1c00, v88
	ds_read_b128 v[0:3], v103
	ds_read_b128 v[4:7], v103 offset:1024
	ds_read_b128 v[8:11], v103 offset:2048
	ds_read_b128 v[12:15], v103 offset:3072
	ds_read_b128 v[16:19], v103 offset:4096
	ds_read_b128 v[20:23], v103 offset:5120
	ds_read_b128 v[24:27], v103 offset:6144
	ds_read_b128 v[28:31], v103 offset:7168
	s_mov_b64 exec, s[24:25]
	s_waitcnt lgkmcnt(7)
	global_store_dwordx4 v104, v[0:3], s[8:9] nt
	s_waitcnt lgkmcnt(6)
	global_store_dwordx4 v105, v[4:7], s[8:9] nt
	s_waitcnt lgkmcnt(5)
	global_store_dwordx4 v106, v[8:11], s[8:9] nt
	s_waitcnt lgkmcnt(4)
	global_store_dwordx4 v107, v[12:15], s[8:9] nt
	s_waitcnt lgkmcnt(3)
	global_store_dwordx4 v108, v[16:19], s[8:9] nt
	s_waitcnt lgkmcnt(2)
	global_store_dwordx4 v109, v[20:23], s[8:9] nt
	s_waitcnt lgkmcnt(1)
	global_store_dwordx4 v110, v[24:27], s[8:9] nt
	s_waitcnt lgkmcnt(0)
	global_store_dwordx4 v111, v[28:31], s[8:9] nt
	s_mov_b64 exec, -1
	s_waitcnt vmcnt(8)
	s_add_u32 s8, s8, 0x61a800
	s_addc_u32 s9, s9, 0
	s_add_i32 s0, s0, 1
	s_cmp_lt_u32 s0, 8
	s_cbranch_scc1 .Lfc_step
	s_cmp_eq_u32 s20, 15
	s_cbranch_scc1 .Lfc_exit
	s_waitcnt vmcnt(8)
	s_barrier
	s_add_i32 s20, s20, 1
	s_branch .Lfc_seg
